# baseline (speedup 1.0000x reference)
.Llight_loop:
	v_mfma_f32_32x32x16_bf16 v[18:33], v[78:81], v[130:133], v[18:33]
	ds_read_b128 v[82:85], v234 offset:128
	ds_read_b128 v[86:89], v234 offset:144
	ds_read_b128 v[90:93], v234 offset:160
	ds_read_b128 v[94:97], v234 offset:176
	ds_read2_b32 v[244:245], v232 offset1:32
	v_exp_f32_e32 v212, v4
	v_exp_f32_e32 v213, v8
	v_exp_f32_e32 v214, v12
	v_exp_f32_e32 v215, v16
	s_waitcnt lgkmcnt(5)
	s_barrier
	v_exp_f32_e32 v217, v2
	v_fma_f32 v251, v212, s12, s12
	v_exp_f32_e32 v218, v6
	v_fma_f32 v252, v213, s12, s12
	v_exp_f32_e32 v219, v10
	v_fma_f32 v253, v214, s12, s12
	v_exp_f32_e32 v220, v14
	v_fma_f32 v254, v215, s12, s12
	v_mfma_f32_32x32x16_bf16 v[18:33], v[74:77], v[134:137], v[18:33]
	ds_read_b128 v[162:165], v210 offset:8192
	ds_read_b128 v[166:169], v210 offset:9216
	v_exp_f32_e32 v221, v3
	v_fmac_f32_e32 v251, v217, v251
	v_exp_f32_e32 v222, v7
	v_fmac_f32_e32 v252, v218, v252
	v_exp_f32_e32 v223, v11
	v_fmac_f32_e32 v253, v219, v253
	v_exp_f32_e32 v224, v15
	v_fmac_f32_e32 v254, v220, v254
	v_mfma_f32_32x32x16_bf16 v[18:33], v[70:73], v[138:141], v[18:33]
	ds_read_b128 v[170:173], v210 offset:10240
	ds_read_b128 v[174:177], v210 offset:11264
	v_rcp_f32_e32 v217, v251
	v_add_f32_e32 v221, 1.0, v221
	v_rcp_f32_e32 v218, v252
	v_add_f32_e32 v222, 1.0, v222
	v_rcp_f32_e32 v219, v253
	v_add_f32_e32 v223, 1.0, v223
	v_rcp_f32_e32 v220, v254
	v_add_f32_e32 v224, 1.0, v224
	v_mfma_f32_32x32x16_bf16 v[18:33], v[66:69], v[142:145], v[18:33]
	ds_read_b128 v[178:181], v210 offset:12288
	ds_read_b128 v[182:185], v210 offset:13312
	v_rcp_f32_e32 v221, v221
	v_fma_f32 v240, -v212, v217, v217
	v_rcp_f32_e32 v222, v222
	v_fma_f32 v241, -v213, v218, v218
	v_rcp_f32_e32 v223, v223
	v_fma_f32 v242, -v214, v219, v219
	v_rcp_f32_e32 v224, v224
	v_fma_f32 v243, -v215, v220, v220
	v_mfma_f32_32x32x16_bf16 v[18:33], v[62:65], v[146:149], v[18:33]
	ds_read_b128 v[186:189], v210 offset:14336
	ds_read_b128 v[190:193], v210 offset:15360
	v_exp_f32_e32 v246, v5
	v_fma_f32 v194, v221, v194, v240
	v_exp_f32_e32 v247, v9
	v_fma_f32 v195, v222, v195, v241
	v_exp_f32_e32 v248, v13
	v_fma_f32 v196, v223, v196, v242
	v_exp_f32_e32 v249, v17
	v_fma_f32 v197, v224, v197, v243
	v_mfma_f32_32x32x16_bf16 v[18:33], v[58:61], v[150:153], v[18:33]
	v_exp_f32_e32 v212, v194
	v_add_f32_e32 v246, 1.0, v246
	v_exp_f32_e32 v213, v195
	v_add_f32_e32 v247, 1.0, v247
	v_exp_f32_e32 v214, v196
	v_add_f32_e32 v248, 1.0, v248
	v_exp_f32_e32 v215, v197
	v_add_f32_e32 v249, 1.0, v249
	v_fmac_f32_e32 v246, v246, v212
	v_fmac_f32_e32 v247, v247, v213
	v_fmac_f32_e32 v248, v248, v214
	v_fmac_f32_e32 v249, v249, v215
	v_mfma_f32_32x32x16_bf16 v[18:33], v[54:57], v[154:157], v[18:33]
	v_rcp_f32_e32 v246, v246
	v_rcp_f32_e32 v247, v247
	v_rcp_f32_e32 v248, v248
	v_rcp_f32_e32 v249, v249
	v_fma_f32 v246, -v212, v246, v246
	v_fma_f32 v247, -v213, v247, v247
	v_fma_f32 v248, -v214, v248, v248
	v_fma_f32 v249, -v215, v249, v249
	v_mfma_f32_32x32x16_bf16 v[18:33], v[50:53], v[158:161], v[18:33]
	s_nop 1
	v_cvt_pk_bf16_f32 v236, v246, v247
	v_cvt_pk_bf16_f32 v237, v248, v249
	s_waitcnt lgkmcnt(0)
	v_mfma_f32_32x32x16_bf16 v[34:49], v[126:129], v[162:165], v[34:49]
	v_add_u32_e32 v233, v231, v244
	ds_read_b128 v[2:5], v233 offset:0
	ds_read_b128 v[6:9], v233 offset:16
	ds_read_b128 v[10:13], v233 offset:32
	ds_read_b128 v[14:17], v233 offset:48
	v_exp_f32_e32 v212, v20
	v_exp_f32_e32 v213, v24
	v_exp_f32_e32 v214, v28
	v_exp_f32_e32 v215, v32
	v_mfma_f32_32x32x16_bf16 v[34:49], v[122:125], v[166:169], v[34:49]
	v_exp_f32_e32 v217, v18
	v_fma_f32 v251, v212, s12, s12
	v_exp_f32_e32 v218, v22
	v_fma_f32 v252, v213, s12, s12
	v_exp_f32_e32 v219, v26
	v_fma_f32 v253, v214, s12, s12
	v_exp_f32_e32 v220, v30
	v_fma_f32 v254, v215, s12, s12
	v_mfma_f32_32x32x16_bf16 v[34:49], v[118:121], v[170:173], v[34:49]
	v_exp_f32_e32 v221, v19
	v_fmac_f32_e32 v251, v217, v251
	v_exp_f32_e32 v222, v23
	v_fmac_f32_e32 v252, v218, v252
	v_exp_f32_e32 v223, v27
	v_fmac_f32_e32 v253, v219, v253
	v_exp_f32_e32 v224, v31
	v_fmac_f32_e32 v254, v220, v254
	v_mfma_f32_32x32x16_bf16 v[34:49], v[114:117], v[174:177], v[34:49]
	v_rcp_f32_e32 v217, v251
	v_add_f32_e32 v221, 1.0, v221
	v_rcp_f32_e32 v218, v252
	v_add_f32_e32 v222, 1.0, v222
	v_rcp_f32_e32 v219, v253
	v_add_f32_e32 v223, 1.0, v223
	v_rcp_f32_e32 v220, v254
	v_add_f32_e32 v224, 1.0, v224
	v_mfma_f32_32x32x16_bf16 v[34:49], v[110:113], v[178:181], v[34:49]
	v_rcp_f32_e32 v221, v221
	v_fma_f32 v240, -v212, v217, v217
	v_rcp_f32_e32 v222, v222
	v_fma_f32 v241, -v213, v218, v218
	v_rcp_f32_e32 v223, v223
	v_fma_f32 v242, -v214, v219, v219
	v_rcp_f32_e32 v224, v224
	v_fma_f32 v243, -v215, v220, v220
	v_mfma_f32_32x32x16_bf16 v[34:49], v[106:109], v[182:185], v[34:49]
	v_exp_f32_e32 v246, v21
	v_fma_f32 v198, v221, v198, v240
	v_exp_f32_e32 v247, v25
	v_fma_f32 v199, v222, v199, v241
	v_exp_f32_e32 v248, v29
	v_fma_f32 v200, v223, v200, v242
	v_exp_f32_e32 v249, v33
	v_fma_f32 v201, v224, v201, v243
	v_mfma_f32_32x32x16_bf16 v[34:49], v[102:105], v[186:189], v[34:49]
	v_exp_f32_e32 v212, v198
	v_add_f32_e32 v246, 1.0, v246
	v_exp_f32_e32 v213, v199
	v_add_f32_e32 v247, 1.0, v247
	v_exp_f32_e32 v214, v200
	v_add_f32_e32 v248, 1.0, v248
	v_exp_f32_e32 v215, v201
	v_add_f32_e32 v249, 1.0, v249
	v_fmac_f32_e32 v246, v246, v212
	v_fmac_f32_e32 v247, v247, v213
	v_fmac_f32_e32 v248, v248, v214
	v_fmac_f32_e32 v249, v249, v215
	v_mfma_f32_32x32x16_bf16 v[34:49], v[98:101], v[190:193], v[34:49]
	v_rcp_f32_e32 v246, v246
	v_rcp_f32_e32 v247, v247
	v_rcp_f32_e32 v248, v248
	v_rcp_f32_e32 v249, v249
	v_fma_f32 v246, -v212, v246, v246
	v_fma_f32 v247, -v213, v247, v247
	v_fma_f32 v248, -v214, v248, v248
	v_fma_f32 v249, -v215, v249, v249
	v_cvt_pk_bf16_f32 v238, v246, v247
	v_cvt_pk_bf16_f32 v239, v248, v249
	ds_write_b128 v211, v[236:239] offset:0
	v_mfma_f32_32x32x16_bf16 v[82:97], v[78:81], v[162:165], v[82:97]
	ds_read_b128 v[18:21], v233 offset:128
	ds_read_b128 v[22:25], v233 offset:144
	ds_read_b128 v[26:29], v233 offset:160
	ds_read_b128 v[30:33], v233 offset:176
	v_exp_f32_e32 v212, v36
	v_exp_f32_e32 v213, v40
	v_exp_f32_e32 v214, v44
	v_exp_f32_e32 v215, v48
	s_waitcnt lgkmcnt(4)
	s_barrier
	v_exp_f32_e32 v217, v34
	v_fma_f32 v251, v212, s12, s12
	v_exp_f32_e32 v218, v38
	v_fma_f32 v252, v213, s12, s12
	v_exp_f32_e32 v219, v42
	v_fma_f32 v253, v214, s12, s12
	v_exp_f32_e32 v220, v46
	v_fma_f32 v254, v215, s12, s12
	v_mfma_f32_32x32x16_bf16 v[82:97], v[74:77], v[166:169], v[82:97]
	ds_read_b128 v[130:133], v210 offset:0
	ds_read_b128 v[134:137], v210 offset:1024
	v_exp_f32_e32 v221, v35
	v_fmac_f32_e32 v251, v217, v251
	v_exp_f32_e32 v222, v39
	v_fmac_f32_e32 v252, v218, v252
	v_exp_f32_e32 v223, v43
	v_fmac_f32_e32 v253, v219, v253
	v_exp_f32_e32 v224, v47
	v_fmac_f32_e32 v254, v220, v254
	v_mfma_f32_32x32x16_bf16 v[82:97], v[70:73], v[170:173], v[82:97]
	ds_read_b128 v[138:141], v210 offset:2048
	ds_read_b128 v[142:145], v210 offset:3072
	v_rcp_f32_e32 v217, v251
	v_add_f32_e32 v221, 1.0, v221
	v_rcp_f32_e32 v218, v252
	v_add_f32_e32 v222, 1.0, v222
	v_rcp_f32_e32 v219, v253
	v_add_f32_e32 v223, 1.0, v223
	v_rcp_f32_e32 v220, v254
	v_add_f32_e32 v224, 1.0, v224
	v_mfma_f32_32x32x16_bf16 v[82:97], v[66:69], v[174:177], v[82:97]
	ds_read_b128 v[146:149], v210 offset:4096
	ds_read_b128 v[150:153], v210 offset:5120
	v_rcp_f32_e32 v221, v221
	v_fma_f32 v240, -v212, v217, v217
	v_rcp_f32_e32 v222, v222
	v_fma_f32 v241, -v213, v218, v218
	v_rcp_f32_e32 v223, v223
	v_fma_f32 v242, -v214, v219, v219
	v_rcp_f32_e32 v224, v224
	v_fma_f32 v243, -v215, v220, v220
	v_mfma_f32_32x32x16_bf16 v[82:97], v[62:65], v[178:181], v[82:97]
	ds_read_b128 v[154:157], v210 offset:6144
	ds_read_b128 v[158:161], v210 offset:7168
	v_exp_f32_e32 v246, v37
	v_fma_f32 v202, v221, v202, v240
	v_exp_f32_e32 v247, v41
	v_fma_f32 v203, v222, v203, v241
	v_exp_f32_e32 v248, v45
	v_fma_f32 v204, v223, v204, v242
	v_exp_f32_e32 v249, v49
	v_fma_f32 v205, v224, v205, v243
	v_mfma_f32_32x32x16_bf16 v[82:97], v[58:61], v[182:185], v[82:97]
	v_exp_f32_e32 v212, v202
	v_add_f32_e32 v246, 1.0, v246
	v_exp_f32_e32 v213, v203
	v_add_f32_e32 v247, 1.0, v247
	v_exp_f32_e32 v214, v204
	v_add_f32_e32 v248, 1.0, v248
	v_exp_f32_e32 v215, v205
	v_add_f32_e32 v249, 1.0, v249
	v_fmac_f32_e32 v246, v246, v212
	v_fmac_f32_e32 v247, v247, v213
	v_fmac_f32_e32 v248, v248, v214
	v_fmac_f32_e32 v249, v249, v215
	v_mfma_f32_32x32x16_bf16 v[82:97], v[54:57], v[186:189], v[82:97]
	v_rcp_f32_e32 v246, v246
	v_rcp_f32_e32 v247, v247
	v_rcp_f32_e32 v248, v248
	v_rcp_f32_e32 v249, v249
	v_fma_f32 v246, -v212, v246, v246
	v_fma_f32 v247, -v213, v247, v247
	v_fma_f32 v248, -v214, v248, v248
	v_fma_f32 v249, -v215, v249, v249
	v_mfma_f32_32x32x16_bf16 v[82:97], v[50:53], v[190:193], v[82:97]
	s_nop 1
	v_cvt_pk_bf16_f32 v236, v246, v247
	v_cvt_pk_bf16_f32 v237, v248, v249
	s_waitcnt lgkmcnt(0)
	v_mfma_f32_32x32x16_bf16 v[2:17], v[126:129], v[130:133], v[2:17]
	v_add_u32_e32 v234, v231, v245
	ds_read_b128 v[34:37], v234 offset:0
	ds_read_b128 v[38:41], v234 offset:16
	ds_read_b128 v[42:45], v234 offset:32
	ds_read_b128 v[46:49], v234 offset:48
	v_add_u32_e32 v232, 0x100, v232
	v_exp_f32_e32 v212, v84
	v_exp_f32_e32 v213, v88
	v_exp_f32_e32 v214, v92
	v_exp_f32_e32 v215, v96
	v_mfma_f32_32x32x16_bf16 v[2:17], v[122:125], v[134:137], v[2:17]
	v_exp_f32_e32 v217, v82
	v_fma_f32 v251, v212, s12, s12
	v_exp_f32_e32 v218, v86
	v_fma_f32 v252, v213, s12, s12
	v_exp_f32_e32 v219, v90
	v_fma_f32 v253, v214, s12, s12
	v_exp_f32_e32 v220, v94
	v_fma_f32 v254, v215, s12, s12
	v_mfma_f32_32x32x16_bf16 v[2:17], v[118:121], v[138:141], v[2:17]
	v_exp_f32_e32 v221, v83
	v_fmac_f32_e32 v251, v217, v251
	v_exp_f32_e32 v222, v87
	v_fmac_f32_e32 v252, v218, v252
	v_exp_f32_e32 v223, v91
	v_fmac_f32_e32 v253, v219, v253
	v_exp_f32_e32 v224, v95
	v_fmac_f32_e32 v254, v220, v254
	v_mfma_f32_32x32x16_bf16 v[2:17], v[114:117], v[142:145], v[2:17]
	v_rcp_f32_e32 v217, v251
	v_add_f32_e32 v221, 1.0, v221
	v_rcp_f32_e32 v218, v252
	v_add_f32_e32 v222, 1.0, v222
	v_rcp_f32_e32 v219, v253
	v_add_f32_e32 v223, 1.0, v223
	v_rcp_f32_e32 v220, v254
	v_add_f32_e32 v224, 1.0, v224
	v_mfma_f32_32x32x16_bf16 v[2:17], v[110:113], v[146:149], v[2:17]
	v_rcp_f32_e32 v221, v221
	v_fma_f32 v240, -v212, v217, v217
	v_rcp_f32_e32 v222, v222
	v_fma_f32 v241, -v213, v218, v218
	v_rcp_f32_e32 v223, v223
	v_fma_f32 v242, -v214, v219, v219
	v_rcp_f32_e32 v224, v224
	v_fma_f32 v243, -v215, v220, v220
	v_mfma_f32_32x32x16_bf16 v[2:17], v[106:109], v[150:153], v[2:17]
	v_exp_f32_e32 v246, v85
	v_fma_f32 v206, v221, v206, v240
	v_exp_f32_e32 v247, v89
	v_fma_f32 v207, v222, v207, v241
	v_exp_f32_e32 v248, v93
	v_fma_f32 v208, v223, v208, v242
	v_exp_f32_e32 v249, v97
	v_fma_f32 v209, v224, v209, v243
	v_mfma_f32_32x32x16_bf16 v[2:17], v[102:105], v[154:157], v[2:17]
	v_exp_f32_e32 v212, v206
	v_add_f32_e32 v246, 1.0, v246
	v_exp_f32_e32 v213, v207
	v_add_f32_e32 v247, 1.0, v247
	v_exp_f32_e32 v214, v208
	v_add_f32_e32 v248, 1.0, v248
	v_exp_f32_e32 v215, v209
	v_add_f32_e32 v249, 1.0, v249
	v_fmac_f32_e32 v246, v246, v212
	v_fmac_f32_e32 v247, v247, v213
	v_fmac_f32_e32 v248, v248, v214
	v_fmac_f32_e32 v249, v249, v215
	v_mfma_f32_32x32x16_bf16 v[2:17], v[98:101], v[158:161], v[2:17]
	v_rcp_f32_e32 v246, v246
	v_rcp_f32_e32 v247, v247
	v_rcp_f32_e32 v248, v248
	v_rcp_f32_e32 v249, v249
	v_fma_f32 v246, -v212, v246, v246
	v_fma_f32 v247, -v213, v247, v247
	v_fma_f32 v248, -v214, v248, v248
	v_fma_f32 v249, -v215, v249, v249
	v_cvt_pk_bf16_f32 v238, v246, v247
	v_cvt_pk_bf16_f32 v239, v248, v249
	ds_write_b128 v211, v[236:239] offset:8192
	s_sub_u32 s16, s16, 1
	s_cmp_lg_u32 s16, 0
	s_cbranch_scc1 .Llight_loop
	v_mfma_f32_32x32x16_bf16 v[18:33], v[78:81], v[130:133], v[18:33]
	ds_read_b128 v[82:85], v234 offset:128
	ds_read_b128 v[86:89], v234 offset:144
	ds_read_b128 v[90:93], v234 offset:160
	ds_read_b128 v[94:97], v234 offset:176
	v_exp_f32_e32 v212, v4
	v_exp_f32_e32 v213, v8
	v_exp_f32_e32 v214, v12
	v_exp_f32_e32 v215, v16
	s_waitcnt lgkmcnt(4)
	s_barrier
	v_exp_f32_e32 v217, v2
	v_fma_f32 v251, v212, s12, s12
	v_exp_f32_e32 v218, v6
	v_fma_f32 v252, v213, s12, s12
	v_exp_f32_e32 v219, v10
	v_fma_f32 v253, v214, s12, s12
	v_exp_f32_e32 v220, v14
	v_fma_f32 v254, v215, s12, s12
	v_mfma_f32_32x32x16_bf16 v[18:33], v[74:77], v[134:137], v[18:33]
	ds_read_b128 v[162:165], v210 offset:8192
	ds_read_b128 v[166:169], v210 offset:9216
	v_exp_f32_e32 v221, v3
	v_fmac_f32_e32 v251, v217, v251
	v_exp_f32_e32 v222, v7
	v_fmac_f32_e32 v252, v218, v252
	v_exp_f32_e32 v223, v11
	v_fmac_f32_e32 v253, v219, v253
	v_exp_f32_e32 v224, v15
	v_fmac_f32_e32 v254, v220, v254
	v_mfma_f32_32x32x16_bf16 v[18:33], v[70:73], v[138:141], v[18:33]
	ds_read_b128 v[170:173], v210 offset:10240
	ds_read_b128 v[174:177], v210 offset:11264
	v_rcp_f32_e32 v217, v251
	v_add_f32_e32 v221, 1.0, v221
	v_rcp_f32_e32 v218, v252
	v_add_f32_e32 v222, 1.0, v222
	v_rcp_f32_e32 v219, v253
	v_add_f32_e32 v223, 1.0, v223
	v_rcp_f32_e32 v220, v254
	v_add_f32_e32 v224, 1.0, v224
	v_mfma_f32_32x32x16_bf16 v[18:33], v[66:69], v[142:145], v[18:33]
	ds_read_b128 v[178:181], v210 offset:12288
	ds_read_b128 v[182:185], v210 offset:13312
	v_rcp_f32_e32 v221, v221
	v_fma_f32 v240, -v212, v217, v217
	v_rcp_f32_e32 v222, v222
	v_fma_f32 v241, -v213, v218, v218
	v_rcp_f32_e32 v223, v223
	v_fma_f32 v242, -v214, v219, v219
	v_rcp_f32_e32 v224, v224
	v_fma_f32 v243, -v215, v220, v220
	v_mfma_f32_32x32x16_bf16 v[18:33], v[62:65], v[146:149], v[18:33]
	ds_read_b128 v[186:189], v210 offset:14336
	ds_read_b128 v[190:193], v210 offset:15360
	v_exp_f32_e32 v246, v5
	v_fma_f32 v194, v221, v194, v240
	v_exp_f32_e32 v247, v9
	v_fma_f32 v195, v222, v195, v241
	v_exp_f32_e32 v248, v13
	v_fma_f32 v196, v223, v196, v242
	v_exp_f32_e32 v249, v17
	v_fma_f32 v197, v224, v197, v243
	v_mfma_f32_32x32x16_bf16 v[18:33], v[58:61], v[150:153], v[18:33]
	v_exp_f32_e32 v212, v194
	v_add_f32_e32 v246, 1.0, v246
	v_exp_f32_e32 v213, v195
	v_add_f32_e32 v247, 1.0, v247
	v_exp_f32_e32 v214, v196
	v_add_f32_e32 v248, 1.0, v248
	v_exp_f32_e32 v215, v197
	v_add_f32_e32 v249, 1.0, v249
	v_fmac_f32_e32 v246, v246, v212
	v_fmac_f32_e32 v247, v247, v213
	v_fmac_f32_e32 v248, v248, v214
	v_fmac_f32_e32 v249, v249, v215
	v_mfma_f32_32x32x16_bf16 v[18:33], v[54:57], v[154:157], v[18:33]
	v_rcp_f32_e32 v246, v246
	v_rcp_f32_e32 v247, v247
	v_rcp_f32_e32 v248, v248
	v_rcp_f32_e32 v249, v249
	v_fma_f32 v246, -v212, v246, v246
	v_fma_f32 v247, -v213, v247, v247
	v_fma_f32 v248, -v214, v248, v248
	v_fma_f32 v249, -v215, v249, v249
	v_mfma_f32_32x32x16_bf16 v[18:33], v[50:53], v[158:161], v[18:33]
	s_nop 1
	v_cvt_pk_bf16_f32 v236, v246, v247
	v_cvt_pk_bf16_f32 v237, v248, v249
	s_waitcnt lgkmcnt(0)
	v_mfma_f32_32x32x16_bf16 v[34:49], v[126:129], v[162:165], v[34:49]
	v_exp_f32_e32 v212, v20
	v_exp_f32_e32 v213, v24
	v_exp_f32_e32 v214, v28
	v_exp_f32_e32 v215, v32
	v_mfma_f32_32x32x16_bf16 v[34:49], v[122:125], v[166:169], v[34:49]
	v_exp_f32_e32 v217, v18
	v_fma_f32 v251, v212, s12, s12
	v_exp_f32_e32 v218, v22
	v_fma_f32 v252, v213, s12, s12
	v_exp_f32_e32 v219, v26
	v_fma_f32 v253, v214, s12, s12
	v_exp_f32_e32 v220, v30
	v_fma_f32 v254, v215, s12, s12
	v_mfma_f32_32x32x16_bf16 v[34:49], v[118:121], v[170:173], v[34:49]
	v_exp_f32_e32 v221, v19
	v_fmac_f32_e32 v251, v217, v251
	v_exp_f32_e32 v222, v23
	v_fmac_f32_e32 v252, v218, v252
	v_exp_f32_e32 v223, v27
	v_fmac_f32_e32 v253, v219, v253
	v_exp_f32_e32 v224, v31
	v_fmac_f32_e32 v254, v220, v254
	v_mfma_f32_32x32x16_bf16 v[34:49], v[114:117], v[174:177], v[34:49]
	v_rcp_f32_e32 v217, v251
	v_add_f32_e32 v221, 1.0, v221
	v_rcp_f32_e32 v218, v252
	v_add_f32_e32 v222, 1.0, v222
	v_rcp_f32_e32 v219, v253
	v_add_f32_e32 v223, 1.0, v223
	v_rcp_f32_e32 v220, v254
	v_add_f32_e32 v224, 1.0, v224
	v_mfma_f32_32x32x16_bf16 v[34:49], v[110:113], v[178:181], v[34:49]
	v_rcp_f32_e32 v221, v221
	v_fma_f32 v240, -v212, v217, v217
	v_rcp_f32_e32 v222, v222
	v_fma_f32 v241, -v213, v218, v218
	v_rcp_f32_e32 v223, v223
	v_fma_f32 v242, -v214, v219, v219
	v_rcp_f32_e32 v224, v224
	v_fma_f32 v243, -v215, v220, v220
	v_mfma_f32_32x32x16_bf16 v[34:49], v[106:109], v[182:185], v[34:49]
	v_exp_f32_e32 v246, v21
	v_fma_f32 v198, v221, v198, v240
	v_exp_f32_e32 v247, v25
	v_fma_f32 v199, v222, v199, v241
	v_exp_f32_e32 v248, v29
	v_fma_f32 v200, v223, v200, v242
	v_exp_f32_e32 v249, v33
	v_fma_f32 v201, v224, v201, v243
	v_mfma_f32_32x32x16_bf16 v[34:49], v[102:105], v[186:189], v[34:49]
	v_exp_f32_e32 v212, v198
	v_add_f32_e32 v246, 1.0, v246
	v_exp_f32_e32 v213, v199
	v_add_f32_e32 v247, 1.0, v247
	v_exp_f32_e32 v214, v200
	v_add_f32_e32 v248, 1.0, v248
	v_exp_f32_e32 v215, v201
	v_add_f32_e32 v249, 1.0, v249
	v_fmac_f32_e32 v246, v246, v212
	v_fmac_f32_e32 v247, v247, v213
	v_fmac_f32_e32 v248, v248, v214
	v_fmac_f32_e32 v249, v249, v215
	v_mfma_f32_32x32x16_bf16 v[34:49], v[98:101], v[190:193], v[34:49]
	v_rcp_f32_e32 v246, v246
	v_rcp_f32_e32 v247, v247
	v_rcp_f32_e32 v248, v248
	v_rcp_f32_e32 v249, v249
	v_fma_f32 v246, -v212, v246, v246
	v_fma_f32 v247, -v213, v247, v247
	v_fma_f32 v248, -v214, v248, v248
	v_fma_f32 v249, -v215, v249, v249
	v_cvt_pk_bf16_f32 v238, v246, v247
	v_cvt_pk_bf16_f32 v239, v248, v249
	ds_write_b128 v211, v[236:239] offset:0
	s_waitcnt lgkmcnt(0)
	s_barrier
	s_bfe_u32 s20, s19, 0x10006
	s_lshl_b32 s21, s20, 7
	s_lshl_b32 s20, s20, 13
	s_add_u32 s20, s20, 0x30000
	s_add_u32 s22, s14, s20
	s_addc_u32 s23, s15, 0
	s_add_u32 s24, s22, 0x1000
	s_addc_u32 s25, s23, 0
	global_load_dwordx4 v[98:101], v210, s[22:23] offset:0
	global_load_dwordx4 v[102:105], v210, s[22:23] offset:1024
	global_load_dwordx4 v[106:109], v210, s[22:23] offset:2048
	global_load_dwordx4 v[110:113], v210, s[22:23] offset:3072
	global_load_dwordx4 v[114:117], v210, s[24:25] offset:0
	global_load_dwordx4 v[118:121], v210, s[24:25] offset:1024
	global_load_dwordx4 v[122:125], v210, s[24:25] offset:2048
	global_load_dwordx4 v[126:129], v210, s[24:25] offset:3072
	v_or_b32_e32 v250, s21, v230
	global_load_dwordx4 v[130:133], v250, s[4:5] offset:0
	global_load_dwordx4 v[134:137], v250, s[4:5] offset:32
	global_load_dwordx4 v[138:141], v250, s[4:5] offset:64
	global_load_dwordx4 v[142:145], v250, s[4:5] offset:96
	global_load_dwordx4 v[146:149], v250, s[6:7] offset:0
	global_load_dwordx4 v[150:153], v250, s[6:7] offset:32
	global_load_dwordx4 v[154:157], v250, s[6:7] offset:64
	global_load_dwordx4 v[158:161], v250, s[6:7] offset:96
	s_load_dword s26, s[8:9], 0x0
	v_mfma_f32_32x32x16_bf16 v[82:97], v[78:81], v[162:165], v[82:97]
	v_exp_f32_e32 v212, v36
	v_exp_f32_e32 v213, v40
	v_exp_f32_e32 v214, v44
	v_exp_f32_e32 v215, v48
	v_mfma_f32_32x32x16_bf16 v[82:97], v[74:77], v[166:169], v[82:97]
	v_exp_f32_e32 v217, v34
	v_fma_f32 v251, v212, s12, s12
	v_exp_f32_e32 v218, v38
	v_fma_f32 v252, v213, s12, s12
	v_exp_f32_e32 v219, v42
	v_fma_f32 v253, v214, s12, s12
	v_exp_f32_e32 v220, v46
	v_fma_f32 v254, v215, s12, s12
	v_mfma_f32_32x32x16_bf16 v[82:97], v[70:73], v[170:173], v[82:97]
	v_exp_f32_e32 v221, v35
	v_fmac_f32_e32 v251, v217, v251
	v_exp_f32_e32 v222, v39
	v_fmac_f32_e32 v252, v218, v252
	v_exp_f32_e32 v223, v43
	v_fmac_f32_e32 v253, v219, v253
	v_exp_f32_e32 v224, v47
	v_fmac_f32_e32 v254, v220, v254
	v_mfma_f32_32x32x16_bf16 v[82:97], v[66:69], v[174:177], v[82:97]
	v_rcp_f32_e32 v217, v251
	v_add_f32_e32 v221, 1.0, v221
	v_rcp_f32_e32 v218, v252
	v_add_f32_e32 v222, 1.0, v222
	v_rcp_f32_e32 v219, v253
	v_add_f32_e32 v223, 1.0, v223
	v_rcp_f32_e32 v220, v254
	v_add_f32_e32 v224, 1.0, v224
	v_mfma_f32_32x32x16_bf16 v[82:97], v[62:65], v[178:181], v[82:97]
	v_rcp_f32_e32 v221, v221
	v_fma_f32 v240, -v212, v217, v217
	v_rcp_f32_e32 v222, v222
	v_fma_f32 v241, -v213, v218, v218
	v_rcp_f32_e32 v223, v223
	v_fma_f32 v242, -v214, v219, v219
	v_rcp_f32_e32 v224, v224
	v_fma_f32 v243, -v215, v220, v220
	v_mfma_f32_32x32x16_bf16 v[82:97], v[58:61], v[182:185], v[82:97]
	v_exp_f32_e32 v246, v37
	v_fma_f32 v202, v221, v202, v240
	v_exp_f32_e32 v247, v41
	v_fma_f32 v203, v222, v203, v241
	v_exp_f32_e32 v248, v45
	v_fma_f32 v204, v223, v204, v242
	v_exp_f32_e32 v249, v49
	v_fma_f32 v205, v224, v205, v243
	v_mfma_f32_32x32x16_bf16 v[82:97], v[54:57], v[186:189], v[82:97]
	v_exp_f32_e32 v212, v202
	v_add_f32_e32 v246, 1.0, v246
	v_exp_f32_e32 v213, v203
	v_add_f32_e32 v247, 1.0, v247
	v_exp_f32_e32 v214, v204
	v_add_f32_e32 v248, 1.0, v248
	v_exp_f32_e32 v215, v205
	v_add_f32_e32 v249, 1.0, v249
	v_fmac_f32_e32 v246, v246, v212
	v_fmac_f32_e32 v247, v247, v213
	v_fmac_f32_e32 v248, v248, v214
	v_fmac_f32_e32 v249, v249, v215
	v_mfma_f32_32x32x16_bf16 v[82:97], v[50:53], v[190:193], v[82:97]
	v_rcp_f32_e32 v246, v246
	v_rcp_f32_e32 v247, v247
	v_rcp_f32_e32 v248, v248
	v_rcp_f32_e32 v249, v249
	v_fma_f32 v246, -v212, v246, v246
	v_fma_f32 v247, -v213, v247, v247
	v_fma_f32 v248, -v214, v248, v248
	v_fma_f32 v249, -v215, v249, v249
	v_cvt_pk_bf16_f32 v236, v246, v247
	v_cvt_pk_bf16_f32 v237, v248, v249
	s_waitcnt lgkmcnt(0)
	v_exp_f32_e32 v212, v84
	v_exp_f32_e32 v213, v88
	v_exp_f32_e32 v214, v92
	v_exp_f32_e32 v215, v96
	v_exp_f32_e32 v217, v82
	v_fma_f32 v251, v212, s12, s12
	v_exp_f32_e32 v218, v86
	v_fma_f32 v252, v213, s12, s12
	v_exp_f32_e32 v219, v90
	v_fma_f32 v253, v214, s12, s12
	v_exp_f32_e32 v220, v94
	v_fma_f32 v254, v215, s12, s12
	v_exp_f32_e32 v221, v83
	v_fmac_f32_e32 v251, v217, v251
	v_exp_f32_e32 v222, v87
	v_fmac_f32_e32 v252, v218, v252
	v_exp_f32_e32 v223, v91
	v_fmac_f32_e32 v253, v219, v253
	v_exp_f32_e32 v224, v95
	v_fmac_f32_e32 v254, v220, v254
	v_rcp_f32_e32 v217, v251
	v_add_f32_e32 v221, 1.0, v221
	v_rcp_f32_e32 v218, v252
	v_add_f32_e32 v222, 1.0, v222
	v_rcp_f32_e32 v219, v253
	v_add_f32_e32 v223, 1.0, v223
	v_rcp_f32_e32 v220, v254
	v_add_f32_e32 v224, 1.0, v224
	v_rcp_f32_e32 v221, v221
	v_fma_f32 v240, -v212, v217, v217
	v_rcp_f32_e32 v222, v222
	v_fma_f32 v241, -v213, v218, v218
	v_rcp_f32_e32 v223, v223
	v_fma_f32 v242, -v214, v219, v219
	v_rcp_f32_e32 v224, v224
	v_fma_f32 v243, -v215, v220, v220
	v_exp_f32_e32 v246, v85
	v_fma_f32 v206, v221, v206, v240
	v_exp_f32_e32 v247, v89
	v_fma_f32 v207, v222, v207, v241
	v_exp_f32_e32 v248, v93
	v_fma_f32 v208, v223, v208, v242
	v_exp_f32_e32 v249, v97
	v_fma_f32 v209, v224, v209, v243
	v_exp_f32_e32 v212, v206
	v_add_f32_e32 v246, 1.0, v246
	v_exp_f32_e32 v213, v207
	v_add_f32_e32 v247, 1.0, v247
	v_exp_f32_e32 v214, v208
	v_add_f32_e32 v248, 1.0, v248
	v_exp_f32_e32 v215, v209
	v_add_f32_e32 v249, 1.0, v249
	v_fmac_f32_e32 v246, v246, v212
	v_fmac_f32_e32 v247, v247, v213
	v_fmac_f32_e32 v248, v248, v214
	v_fmac_f32_e32 v249, v249, v215
	v_rcp_f32_e32 v246, v246
	v_rcp_f32_e32 v247, v247
	v_rcp_f32_e32 v248, v248
	v_rcp_f32_e32 v249, v249
	v_fma_f32 v246, -v212, v246, v246
	v_fma_f32 v247, -v213, v247, v247
	v_fma_f32 v248, -v214, v248, v248
	v_fma_f32 v249, -v215, v249, v249
	v_cvt_pk_bf16_f32 v238, v246, v247
	v_cvt_pk_bf16_f32 v239, v248, v249
	ds_write_b128 v211, v[236:239] offset:8192
	s_waitcnt lgkmcnt(0)
	s_barrier
	s_lshl_b32 s20, s19, 6
	s_and_b32 s20, s20, 0x2000
	v_or_b32_e32 v20, s20, v210
	ds_read_b128 v[162:165], v20 offset:0
	ds_read_b128 v[166:169], v20 offset:1024
	ds_read_b128 v[170:173], v20 offset:2048
	ds_read_b128 v[174:177], v20 offset:3072
	ds_read_b128 v[178:181], v20 offset:4096
	ds_read_b128 v[182:185], v20 offset:5120
	ds_read_b128 v[186:189], v20 offset:6144
	ds_read_b128 v[190:193], v20 offset:7168
	s_bfe_u32 s20, s19, 0x10006
	s_lshl_b32 s20, s20, 9
	s_and_b32 s21, s19, 0x80
	s_or_b32 s20, s20, s21
	v_lshlrev_b32_e32 v19, 2, v229
	v_add3_u32 v19, s20, v19, v228
	s_waitcnt vmcnt(0)
	s_waitcnt lgkmcnt(7)
	v_mfma_f32_32x32x16_bf16 v[2:17], v[98:101], v[162:165], 0
	s_waitcnt lgkmcnt(6)
	v_mfma_f32_32x32x16_bf16 v[2:17], v[102:105], v[166:169], v[2:17]
	s_waitcnt lgkmcnt(5)
	v_mfma_f32_32x32x16_bf16 v[2:17], v[106:109], v[170:173], v[2:17]
	s_waitcnt lgkmcnt(4)
	v_mfma_f32_32x32x16_bf16 v[2:17], v[110:113], v[174:177], v[2:17]
	s_waitcnt lgkmcnt(3)
	v_mfma_f32_32x32x16_bf16 v[2:17], v[114:117], v[178:181], v[2:17]
	s_waitcnt lgkmcnt(2)
	v_mfma_f32_32x32x16_bf16 v[2:17], v[118:121], v[182:185], v[2:17]
	s_waitcnt lgkmcnt(1)
	v_mfma_f32_32x32x16_bf16 v[2:17], v[122:125], v[186:189], v[2:17]
	s_waitcnt lgkmcnt(0)
	v_mfma_f32_32x32x16_bf16 v[2:17], v[126:129], v[190:193], v[2:17]
	s_nop 15
	s_nop 3
	v_add_f32_e32 v2, v2, v130
	v_add_f32_e32 v3, v3, v131
	v_add_f32_e32 v4, v4, v132
	v_add_f32_e32 v5, v5, v133
	v_add_f32_e32 v6, v6, v134
	v_add_f32_e32 v7, v7, v135
	v_add_f32_e32 v8, v8, v136
	v_add_f32_e32 v9, v9, v137
	v_add_f32_e32 v10, v10, v138
	v_add_f32_e32 v11, v11, v139
	v_add_f32_e32 v12, v12, v140
	v_add_f32_e32 v13, v13, v141
	v_add_f32_e32 v14, v14, v142
	v_add_f32_e32 v15, v15, v143
	v_add_f32_e32 v16, v16, v144
	v_add_f32_e32 v17, v17, v145
	v_max_f32_e32 v2, 0, v2
	v_max_f32_e32 v3, 0, v3
	v_max_f32_e32 v4, 0, v4
	v_max_f32_e32 v5, 0, v5
	v_max_f32_e32 v6, 0, v6
	v_max_f32_e32 v7, 0, v7
	v_max_f32_e32 v8, 0, v8
	v_max_f32_e32 v9, 0, v9
	v_max_f32_e32 v10, 0, v10
	v_max_f32_e32 v11, 0, v11
	v_max_f32_e32 v12, 0, v12
	v_max_f32_e32 v13, 0, v13
	v_max_f32_e32 v14, 0, v14
	v_max_f32_e32 v15, 0, v15
	v_max_f32_e32 v16, 0, v16
	v_max_f32_e32 v17, 0, v17
	v_fma_f32 v18, v2, v146, 0
	v_fmac_f32_e32 v18, v3, v147
	v_fmac_f32_e32 v18, v4, v148
	v_fmac_f32_e32 v18, v5, v149
	v_fmac_f32_e32 v18, v6, v150
	v_fmac_f32_e32 v18, v7, v151
	v_fmac_f32_e32 v18, v8, v152
	v_fmac_f32_e32 v18, v9, v153
	v_fmac_f32_e32 v18, v10, v154
	v_fmac_f32_e32 v18, v11, v155
	v_fmac_f32_e32 v18, v12, v156
	v_fmac_f32_e32 v18, v13, v157
	v_fmac_f32_e32 v18, v14, v158
	v_fmac_f32_e32 v18, v15, v159
	v_fmac_f32_e32 v18, v16, v160
	v_fmac_f32_e32 v18, v17, v161
	ds_write_b32 v19, v18 offset:35904
	s_branch .LBB1_40
